# v040 + grid barrier: waiting workgroups sleep ~190 cycles between poll pairs of the release word (less polling traffic while other workgroups are still finishing)
# speedup vs baseline: 1.0034x; 1.0034x over previous
; __device__ __forceinline__ unsigned xb_ld(unsigned* p)              { return __hip_atomic_load(p, __ATOMIC_RELAXED, __HIP_MEMORY_SCOPE_AGENT); }
; __device__ __forceinline__ unsigned xb_add(unsigned* p, unsigned v) { return __hip_atomic_fetch_add(p, v, __ATOMIC_RELAXED, __HIP_MEMORY_SCOPE_AGENT); }
; #define XB_SPIN(cond, bar) do { unsigned _sp = 0; while (cond) { __builtin_amdgcn_s_sleep(1); \
;     if ((++_sp & 255u) == 0u) { if (xb_ld(&(bar)[XB_TMO])) break; if (_sp > XB_SPIN_CAP) { atomicAdd(&(bar)[XB_TMO], 1u); break; } } } } while (0)
; __device__ __forceinline__ void xcd_barrier(const XcdBarrier& b) {
;     ...
;             else XB_SPIN(xb_ld(&bar[XB_TOPGEN]) == tg, bar);
;             __builtin_amdgcn_fence(__ATOMIC_ACQUIRE, "agent");
;             xb_add(&bar[XB_XGEN(b.x)], 1u);
;             asm volatile("s_waitcnt vmcnt(0)" ::: "memory");
;         } else {
;             XB_SPIN(xb_ld(&bar[XB_XGEN(b.x)]) == gen, bar);
.Lbar_nl_poll_12:
	global_load_dword v3, v163, s[8:9] sc1
	s_waitcnt vmcnt(1)
	v_cmp_le_u32_e32 vcc, v16, v2
	s_cbranch_vccnz .Lbar_nl_done_12
	global_load_dword v2, v163, s[8:9] sc1
	s_waitcnt vmcnt(1)
	v_cmp_le_u32_e32 vcc, v16, v3
	s_cbranch_vccnz .Lbar_nl_done_12
	s_sleep 3
	s_add_i32 s20, s20, 1
	s_cmp_lt_u32 s20, 0x20000
	s_cbranch_scc1 .Lbar_nl_poll_12
